# e = p@W kept in GEMM tile/lane order between the prologue GEMM and the PLE gate epilogue (1 KiB contiguous per wave access, writer lane transpose removed)
# speedup vs baseline: 1.0308x; 1.0009x over previous
; __device__ __forceinline__ unsigned pk2(float lo, float hi) { unsigned r; asm("v_cvt_pk_bf16_f32 %0, %1, %2" : "=v"(r) : "v"(lo), "v"(hi)); return r; }
;     __device__ __forceinline__ void operator()(const f32x4 (&acc)[2][2][4][2], const Unit& u, int wr, int wc, int fr, int fq) const {
;         const int lane = fq * 16 + fr, frs = STORE_T ? (lane >> 2) : fr, fqs = STORE_T ? (lane & 3) : fq;
;         const int row0 = u.pm * 256 + wr * 64 + frs, col0 = (u.pn & cmask) * 256 + wc * 32 + 8 * fqs;
; #pragma unroll
;         for (int ai = 0; ai < 2; ++ai)
; #pragma unroll
;             for (int m = 0; m < 4; ++m) { bf16* rowp = O + (size_t)(row0 + ai * 128 + m * 16) * ldc + col0;
; #pragma unroll
;                 for (int bj = 0; bj < 2; ++bj) { const f32x4 v0 = acc[ai][bj][m][0], v1 = acc[ai][bj][m][1];
;                     v4u w; w.x = pk2(v0[0], v0[1]); w.y = pk2(v0[2], v0[3]); w.z = pk2(v1[0], v1[1]); w.w = pk2(v1[2], v1[3]);
;                     if (STORE_T) w = lane_xpose(w, lane);
;                     *(v4u*)(rowp + bj * 128) = w; } }
.LBB0_193:
	v_lshrrev_b32_e32 v220, 6, v0
	v_lshlrev_b32_e32 v220, 14, v220
	v_and_b32_e32 v221, 63, v0
	v_lshl_or_b32 v220, v221, 4, v220
	s_lshl_b32 s98, s28, 2
	s_and_b32 s99, s30, 3
	s_add_i32 s98, s98, s99
	s_lshl_b32 s98, s98, 17
	v_add_u32_e32 v220, s98, v220
	v_mov_b32_e32 v221, 0
	v_lshl_add_u64 v[220:221], s[0:1], 0, v[220:221]
	v_lshl_add_u32 v146, s28, 8, v140
	v_cvt_pk_bf16_f32 v125, v124, v125
	v_cvt_pk_bf16_f32 v109, v108, v109
	s_lshl_b32 s19, s30, 8
	v_cvt_pk_bf16_f32 v126, v126, v127
	v_cvt_pk_bf16_f32 v127, v128, v129
	v_cvt_pk_bf16_f32 v128, v122, v123
	v_mov_b32_e32 v122, v126
	v_mov_b32_e32 v123, v127
	v_mov_b32_e32 v124, v128
	v_mov_b32_e32 v125, v125
	v_cvt_pk_bf16_f32 v118, v118, v119
	v_cvt_pk_bf16_f32 v119, v120, v121
	v_cvt_pk_bf16_f32 v110, v110, v111
	v_cvt_pk_bf16_f32 v111, v112, v113
	v_or_b32_e32 v112, 16, v146
	v_cvt_pk_bf16_f32 v114, v114, v115
	v_cvt_pk_bf16_f32 v115, v116, v117
	v_cvt_pk_bf16_f32 v116, v106, v107
	v_mov_b32_e32 v106, v114
	v_mov_b32_e32 v107, v115
	v_mov_b32_e32 v108, v116
	v_mov_b32_e32 v109, v109
	v_cvt_pk_bf16_f32 v97, v96, v97
	s_and_b32 s19, s19, 0x300
	v_ashrrev_i32_e32 v147, 31, v146
	v_mov_b32_e32 v118, v118
	v_mov_b32_e32 v119, v119
	v_mov_b32_e32 v120, v110
	v_mov_b32_e32 v121, v111
	v_ashrrev_i32_e32 v113, 31, v112
	v_cvt_pk_bf16_f32 v102, v102, v103
	v_cvt_pk_bf16_f32 v103, v104, v105
	v_cvt_pk_bf16_f32 v104, v94, v95
	v_mov_b32_e32 v94, v102
	v_mov_b32_e32 v95, v103
	v_mov_b32_e32 v96, v104
	v_mov_b32_e32 v97, v97
	v_or_b32_e32 v138, s19, v142
	v_lshlrev_b64 v[148:149], 11, v[146:147]
	v_lshlrev_b64 v[102:103], 11, v[112:113]
	v_lshl_add_u64 v[110:111], s[0:1], 0, v[148:149]
	v_lshlrev_b32_e32 v138, 1, v138
	v_lshl_add_u64 v[102:103], s[0:1], 0, v[102:103]
	v_lshl_add_u64 v[110:111], v[110:111], 0, v[138:139]
	v_lshl_add_u64 v[102:103], v[102:103], 0, v[138:139]
	v_cvt_pk_bf16_f32 v93, v92, v93
	s_waitcnt lgkmcnt(0)
	global_store_dwordx4 v[220:221], v[122:125], off
	global_store_dwordx4 v[220:221], v[118:121], off offset:1024
	s_mov_b32 s98, 0x800
	s_mov_b32 s99, 0
	v_lshl_add_u64 v[220:221], v[220:221], 0, s[98:99]
	global_store_dwordx4 v[220:221], v[106:109], off
	global_store_dwordx4 v[220:221], v[94:97], off offset:1024
	v_mov_b32_e32 v93, v93
	v_cvt_pk_bf16_f32 v81, v80, v81
	v_cvt_pk_bf16_f32 v86, v86, v87
	v_cvt_pk_bf16_f32 v87, v88, v89
	v_cvt_pk_bf16_f32 v88, v78, v79
	s_nop 0
	v_or_b32_e32 v94, 32, v146
	v_cvt_pk_bf16_f32 v96, v98, v99
	v_cvt_pk_bf16_f32 v97, v100, v101
	v_cvt_pk_bf16_f32 v98, v90, v91
	v_mov_b32_e32 v90, v96
	v_mov_b32_e32 v91, v97
	v_mov_b32_e32 v92, v98
	v_ashrrev_i32_e32 v95, 31, v94
	v_mov_b32_e32 v78, v86
	v_mov_b32_e32 v79, v87
	v_mov_b32_e32 v80, v88
	v_mov_b32_e32 v81, v81
	v_lshlrev_b64 v[86:87], 11, v[94:95]
	v_lshl_add_u64 v[86:87], s[0:1], 0, v[86:87]
	v_lshl_add_u64 v[86:87], v[86:87], 0, v[138:139]
	v_cvt_pk_bf16_f32 v77, v76, v77
	v_cvt_pk_bf16_f32 v61, v60, v61
	s_waitcnt lgkmcnt(0)
	s_mov_b32 s98, 0x800
	s_mov_b32 s99, 0
	v_lshl_add_u64 v[220:221], v[220:221], 0, s[98:99]
	global_store_dwordx4 v[220:221], v[90:93], off
	global_store_dwordx4 v[220:221], v[78:81], off offset:1024
	v_mov_b32_e32 v77, v77
	v_cvt_pk_bf16_f32 v69, v68, v69
	v_cvt_pk_bf16_f32 v62, v62, v63
	v_cvt_pk_bf16_f32 v63, v64, v65
	v_cvt_pk_bf16_f32 v64, v58, v59
	s_nop 0
	v_or_b32_e32 v78, 48, v146
	v_cvt_pk_bf16_f32 v80, v82, v83
	v_cvt_pk_bf16_f32 v81, v84, v85
	v_cvt_pk_bf16_f32 v82, v74, v75
	v_mov_b32_e32 v74, v80
	v_mov_b32_e32 v75, v81
	v_mov_b32_e32 v76, v82
	v_mov_b32_e32 v58, v62
	v_mov_b32_e32 v59, v63
	v_mov_b32_e32 v60, v64
	v_mov_b32_e32 v61, v61
	v_cvt_pk_bf16_f32 v49, v48, v49
	v_ashrrev_i32_e32 v79, 31, v78
	v_cvt_pk_bf16_f32 v70, v70, v71
	v_cvt_pk_bf16_f32 v71, v72, v73
	v_cvt_pk_bf16_f32 v72, v66, v67
	v_mov_b32_e32 v66, v70
	v_mov_b32_e32 v67, v71
	v_mov_b32_e32 v68, v72
	v_mov_b32_e32 v69, v69
	v_cvt_pk_bf16_f32 v54, v54, v55
	v_cvt_pk_bf16_f32 v55, v56, v57
	v_cvt_pk_bf16_f32 v56, v46, v47
	v_mov_b32_e32 v46, v54
	v_mov_b32_e32 v47, v55
	v_mov_b32_e32 v48, v56
	v_mov_b32_e32 v49, v49
	v_lshlrev_b64 v[70:71], 11, v[78:79]
	v_lshl_add_u64 v[70:71], s[0:1], 0, v[70:71]
	v_add_co_u32_e32 v54, vcc, s67, v110
	v_lshl_add_u64 v[70:71], v[70:71], 0, v[138:139]
	s_nop 0
	v_addc_co_u32_e32 v55, vcc, 0, v111, vcc
	v_cvt_pk_bf16_f32 v45, v44, v45
	s_waitcnt lgkmcnt(0)
; __device__ __forceinline__ unsigned pk2(float lo, float hi) { unsigned r; asm("v_cvt_pk_bf16_f32 %0, %1, %2" : "=v"(r) : "v"(lo), "v"(hi)); return r; }
;     __device__ __forceinline__ void operator()(const f32x4 (&acc)[2][2][4][2], const Unit& u, int wr, int wc, int fr, int fq) const {
;         const int lane = fq * 16 + fr, frs = STORE_T ? (lane >> 2) : fr, fqs = STORE_T ? (lane & 3) : fq;
;         const int row0 = u.pm * 256 + wr * 64 + frs, col0 = (u.pn & cmask) * 256 + wc * 32 + 8 * fqs;
; #pragma unroll
;         for (int ai = 0; ai < 2; ++ai)
; #pragma unroll
;             for (int m = 0; m < 4; ++m) { bf16* rowp = O + (size_t)(row0 + ai * 128 + m * 16) * ldc + col0;
; #pragma unroll
;                 for (int bj = 0; bj < 2; ++bj) { const f32x4 v0 = acc[ai][bj][m][0], v1 = acc[ai][bj][m][1];
;                     v4u w; w.x = pk2(v0[0], v0[1]); w.y = pk2(v0[2], v0[3]); w.z = pk2(v1[0], v1[1]); w.w = pk2(v1[2], v1[3]);
;                     if (STORE_T) w = lane_xpose(w, lane);
;                     *(v4u*)(rowp + bj * 128) = w; } }
	s_mov_b32 s98, 0x800
	s_mov_b32 s99, 0
	v_lshl_add_u64 v[220:221], v[220:221], 0, s[98:99]
	global_store_dwordx4 v[220:221], v[74:77], off
	global_store_dwordx4 v[220:221], v[66:69], off offset:1024
	v_mov_b32_e32 v45, v45
	v_cvt_pk_bf16_f32 v33, v32, v33
	v_cvt_pk_bf16_f32 v38, v38, v39
	v_cvt_pk_bf16_f32 v39, v40, v41
	v_cvt_pk_bf16_f32 v40, v30, v31
	s_nop 0
	v_lshl_add_u64 v[66:67], v[110:111], 0, s[10:11]
	s_mov_b32 s98, 0x800
	s_mov_b32 s99, 0
	v_lshl_add_u64 v[220:221], v[220:221], 0, s[98:99]
	global_store_dwordx4 v[220:221], v[58:61], off
	global_store_dwordx4 v[220:221], v[46:49], off offset:1024
	v_mov_b32_e32 v30, v38
	v_mov_b32_e32 v31, v39
	v_cvt_pk_bf16_f32 v48, v50, v51
	v_cvt_pk_bf16_f32 v49, v52, v53
	v_cvt_pk_bf16_f32 v50, v42, v43
	v_mov_b32_e32 v42, v48
	v_mov_b32_e32 v43, v49
	v_mov_b32_e32 v44, v50
	v_mov_b32_e32 v32, v40
	v_mov_b32_e32 v33, v33
	v_add_co_u32_e32 v38, vcc, s69, v110
	v_cvt_pk_bf16_f32 v29, v28, v29
	v_lshl_add_u64 v[46:47], v[110:111], 0, s[12:13]
	s_nop 0
	v_addc_co_u32_e32 v39, vcc, 0, v111, vcc
	s_waitcnt lgkmcnt(0)
	s_mov_b32 s98, 0x800
	s_mov_b32 s99, 0
	v_lshl_add_u64 v[220:221], v[220:221], 0, s[98:99]
	global_store_dwordx4 v[220:221], v[42:45], off
	global_store_dwordx4 v[220:221], v[30:33], off offset:1024
	v_mov_b32_e32 v29, v29
	v_cvt_pk_bf16_f32 v17, v16, v17
	v_cvt_pk_bf16_f32 v22, v22, v23
	v_cvt_pk_bf16_f32 v23, v24, v25
	v_cvt_pk_bf16_f32 v24, v14, v15
	s_nop 0
	v_cvt_pk_bf16_f32 v32, v34, v35
	v_cvt_pk_bf16_f32 v33, v36, v37
	v_cvt_pk_bf16_f32 v34, v26, v27
	v_mov_b32_e32 v26, v32
	v_mov_b32_e32 v27, v33
	v_mov_b32_e32 v28, v34
	v_mov_b32_e32 v14, v22
	v_mov_b32_e32 v15, v23
	v_mov_b32_e32 v16, v24
	v_mov_b32_e32 v17, v17
	v_add_co_u32_e32 v22, vcc, s70, v110
	v_cvt_pk_bf16_f32 v13, v12, v13
	v_lshl_add_u64 v[30:31], v[110:111], 0, s[14:15]
	s_nop 0
	v_addc_co_u32_e32 v23, vcc, 0, v111, vcc
	s_waitcnt lgkmcnt(0)
	s_mov_b32 s98, 0x800
	s_mov_b32 s99, 0
	v_lshl_add_u64 v[220:221], v[220:221], 0, s[98:99]
	global_store_dwordx4 v[220:221], v[26:29], off
	global_store_dwordx4 v[220:221], v[14:17], off offset:1024
	v_mov_b32_e32 v13, v13
	v_cvt_pk_bf16_f32 v5, v4, v5
	v_cvt_pk_bf16_f32 v6, v6, v7
	v_cvt_pk_bf16_f32 v7, v8, v9
	v_cvt_pk_bf16_f32 v8, v2, v3
	s_nop 0
	v_cvt_pk_bf16_f32 v16, v18, v19
	v_cvt_pk_bf16_f32 v17, v20, v21
	v_cvt_pk_bf16_f32 v18, v10, v11
	v_mov_b32_e32 v10, v16
	v_mov_b32_e32 v11, v17
	v_mov_b32_e32 v12, v18
	v_mov_b32_e32 v2, v6
	v_mov_b32_e32 v3, v7
	v_mov_b32_e32 v4, v8
	v_mov_b32_e32 v5, v5
	v_add_co_u32_e32 v6, vcc, s71, v110
	v_readlane_b32 s76, v253, 4
	s_nop 0
	v_addc_co_u32_e32 v7, vcc, 0, v111, vcc
	s_andn2_b64 vcc, exec, s[22:23]
	s_mov_b64 s[22:23], -1
	v_readlane_b32 s77, v253, 5
	v_lshl_add_u64 v[14:15], v[110:111], 0, s[16:17]
	s_waitcnt lgkmcnt(0)
	s_mov_b32 s98, 0x800
	s_mov_b32 s99, 0
	v_lshl_add_u64 v[220:221], v[220:221], 0, s[98:99]
	global_store_dwordx4 v[220:221], v[10:13], off
	global_store_dwordx4 v[220:221], v[2:5], off offset:1024
	s_cbranch_vccnz .LBB0_186
	s_andn2_b64 vcc, exec, s[4:5]
	s_cbranch_vccnz .LBB0_185
	s_barrier
	s_branch .LBB0_185

; __device__ __forceinline__ unsigned pk2(float lo, float hi) { unsigned r; asm("v_cvt_pk_bf16_f32 %0, %1, %2" : "=v"(r) : "v"(lo), "v"(hi)); return r; }
; __device__ __forceinline__ float bflo(unsigned w) { return __uint_as_float(w << 16); }
; __device__ __forceinline__ float bfhi(unsigned w) { return __uint_as_float(w & 0xffff0000u); }
; __device__ __forceinline__ float sigmoidf_(float x) { return __builtin_amdgcn_rcpf(1.f + __expf(-x)); }
;     __device__ __forceinline__ void operator()(const f32x4 (&acc)[2][2][4][2], const Unit& u, int wr, int wc, int fr, int fq) const {
;         const int row0 = u.pm * 256 + wr * 64 + fr, col0 = u.pn * 256 + wc * 32 + 8 * fq;
; #pragma unroll
;         for (int ai = 0; ai < 2; ++ai)
; #pragma unroll
;             for (int m = 0; m < 4; ++m) { const size_t off = (size_t)(row0 + ai * 128 + m * 16) * D + col0;
; #pragma unroll
;                 for (int bj = 0; bj < 2; ++bj) { const v4u e = __builtin_nontemporal_load((const v4u*)(E + off + bj * 128)); const f32x4 v0 = acc[ai][bj][m][0], v1 = acc[ai][bj][m][1];
;                     v4u w; w.x = pk2(sigmoidf_(v0[0]) * bflo(e.x), sigmoidf_(v0[1]) * bfhi(e.x)); w.y = pk2(sigmoidf_(v0[2]) * bflo(e.y), sigmoidf_(v0[3]) * bfhi(e.y));
;                     w.z = pk2(sigmoidf_(v1[0]) * bflo(e.z), sigmoidf_(v1[1]) * bfhi(e.z)); w.w = pk2(sigmoidf_(v1[2]) * bflo(e.w), sigmoidf_(v1[3]) * bfhi(e.w));
;                     *(v4u*)(GE + off + bj * 128) = w; } }
.LBB0_1515:
	v_lshrrev_b32_e32 v244, 6, v0
	v_lshlrev_b32_e32 v244, 14, v244
	v_and_b32_e32 v245, 63, v0
	v_lshl_or_b32 v244, v245, 4, v244
	s_lshl_b32 s98, s5, 2
	s_add_i32 s98, s98, s4
	s_lshl_b32 s98, s98, 17
	v_add_u32_e32 v244, s98, v244
	v_mov_b32_e32 v245, 0
	v_lshl_add_u64 v[244:245], s[12:13], 0, v[244:245]
	v_lshl_add_u32 v144, s5, 8, v1
	v_lshl_or_b32 v142, s4, 8, v147
	v_ashrrev_i32_e32 v145, 31, v144
	v_ashrrev_i32_e32 v143, 31, v142
	v_lshlrev_b64 v[140:141], 10, v[144:145]
	v_lshl_add_u64 v[140:141], v[140:141], 0, v[142:143]
	v_lshlrev_b64 v[140:141], 1, v[140:141]
	v_lshl_add_u64 v[154:155], s[12:13], 0, v[140:141]
	global_load_dwordx4 v[150:153], v[244:245], off nt
	s_nop 0
	global_load_dwordx4 v[154:157], v[244:245], off offset:1024 nt
	v_mul_f32_e32 v126, 0xbfb8aa3b, v126
	v_mul_f32_e32 v127, 0xbfb8aa3b, v127
	v_mul_f32_e32 v118, 0xbfb8aa3b, v118
	v_mul_f32_e32 v128, 0xbfb8aa3b, v128
	v_mul_f32_e32 v129, 0xbfb8aa3b, v129
	v_mul_f32_e32 v122, 0xbfb8aa3b, v122
	v_mul_f32_e32 v123, 0xbfb8aa3b, v123
	v_mul_f32_e32 v124, 0xbfb8aa3b, v124
	v_mul_f32_e32 v125, 0xbfb8aa3b, v125
	v_mul_f32_e32 v119, 0xbfb8aa3b, v119
	v_mul_f32_e32 v120, 0xbfb8aa3b, v120
	v_mul_f32_e32 v121, 0xbfb8aa3b, v121
	v_mul_f32_e32 v145, 0xbfb8aa3b, v114
	v_exp_f32_e32 v114, v126
	v_exp_f32_e32 v126, v127
	v_exp_f32_e32 v118, v118
	v_exp_f32_e32 v127, v128
	v_exp_f32_e32 v128, v129
	v_exp_f32_e32 v122, v122
	v_exp_f32_e32 v123, v123
	v_exp_f32_e32 v124, v124
	v_exp_f32_e32 v125, v125
	v_exp_f32_e32 v119, v119
	v_exp_f32_e32 v120, v120
	v_exp_f32_e32 v121, v121
	v_add_f32_e32 v114, 1.0, v114
	v_add_f32_e32 v126, 1.0, v126
	v_add_f32_e32 v118, 1.0, v118
	v_add_f32_e32 v127, 1.0, v127
	v_add_f32_e32 v128, 1.0, v128
	v_add_f32_e32 v129, 1.0, v122
	v_add_f32_e32 v149, 1.0, v123
	v_add_f32_e32 v124, 1.0, v124
	v_add_f32_e32 v125, 1.0, v125
	v_add_f32_e32 v119, 1.0, v119
	v_add_f32_e32 v120, 1.0, v120
	v_add_f32_e32 v121, 1.0, v121
	v_rcp_f32_e32 v114, v114
	v_rcp_f32_e32 v126, v126
	v_rcp_f32_e32 v118, v118
	v_rcp_f32_e32 v127, v127
	v_rcp_f32_e32 v128, v128
	v_rcp_f32_e32 v129, v129
	v_rcp_f32_e32 v149, v149
	v_rcp_f32_e32 v124, v124
	v_rcp_f32_e32 v125, v125
	v_rcp_f32_e32 v119, v119
	v_rcp_f32_e32 v120, v120
	v_rcp_f32_e32 v121, v121
	v_lshl_add_u64 v[122:123], s[6:7], 0, v[140:141]
	v_mul_f32_e32 v115, 0xbfb8aa3b, v115
	v_mul_f32_e32 v116, 0xbfb8aa3b, v116
	v_mul_f32_e32 v110, 0xbfb8aa3b, v110
	v_mul_f32_e32 v111, 0xbfb8aa3b, v111
	v_mul_f32_e32 v112, 0xbfb8aa3b, v112
	v_mul_f32_e32 v113, 0xbfb8aa3b, v113
	v_mul_f32_e32 v107, 0xbfb8aa3b, v107
	v_exp_f32_e32 v110, v110
	v_exp_f32_e32 v111, v111
	v_exp_f32_e32 v112, v112
	v_mul_f32_e32 v106, 0xbfb8aa3b, v106
	v_mul_f32_e32 v108, 0xbfb8aa3b, v108
	v_mul_f32_e32 v109, 0xbfb8aa3b, v109
	v_exp_f32_e32 v113, v113
	v_exp_f32_e32 v107, v107
	v_exp_f32_e32 v106, v106
	v_exp_f32_e32 v108, v108
	v_exp_f32_e32 v109, v109
	v_add_f32_e32 v110, 1.0, v110
	v_add_f32_e32 v111, 1.0, v111
	v_add_f32_e32 v112, 1.0, v112
	v_mul_f32_e32 v102, 0xbfb8aa3b, v102
	v_add_f32_e32 v113, 1.0, v113
	v_add_f32_e32 v107, 1.0, v107
	v_rcp_f32_e32 v110, v110
	v_rcp_f32_e32 v111, v111
	v_rcp_f32_e32 v112, v112
	v_exp_f32_e32 v102, v102
	s_waitcnt vmcnt(0)
	v_lshlrev_b32_e32 v158, 16, v150
	v_and_b32_e32 v150, 0xffff0000, v150
	v_lshlrev_b32_e32 v164, 16, v154
	v_lshlrev_b32_e32 v159, 16, v151
	v_and_b32_e32 v151, 0xffff0000, v151
	v_lshlrev_b32_e32 v160, 16, v152
	v_and_b32_e32 v152, 0xffff0000, v152
	v_lshlrev_b32_e32 v161, 16, v153
	v_and_b32_e32 v153, 0xffff0000, v153
	v_and_b32_e32 v154, 0xffff0000, v154
	v_lshlrev_b32_e32 v165, 16, v155
	v_and_b32_e32 v155, 0xffff0000, v155
	v_mul_f32_e32 v114, v114, v158
	v_mul_f32_e32 v126, v126, v150
	v_mul_f32_e32 v150, v118, v164
	v_cvt_pk_bf16_f32 v118, v114, v126
	v_mul_f32_e32 v127, v127, v159
	v_mul_f32_e32 v128, v128, v151
	v_mul_f32_e32 v129, v129, v160
	v_mul_f32_e32 v149, v149, v152
	v_mul_f32_e32 v124, v124, v161
	v_mul_f32_e32 v125, v125, v153
	v_mul_f32_e32 v151, v119, v154
	v_mul_f32_e32 v152, v120, v165
	v_mul_f32_e32 v153, v121, v155
	v_cvt_pk_bf16_f32 v119, v127, v128
	v_cvt_pk_bf16_f32 v120, v129, v149
	v_cvt_pk_bf16_f32 v121, v124, v125
	global_store_dwordx4 v[122:123], v[118:121], off
	v_cvt_pk_bf16_f32 v114, v150, v151
	v_mul_f32_e32 v103, 0xbfb8aa3b, v103
	v_add_f32_e32 v106, 1.0, v106
	v_exp_f32_e32 v118, v145
	v_exp_f32_e32 v119, v115
	v_lshlrev_b32_e32 v120, 16, v156
	v_cvt_pk_bf16_f32 v115, v152, v153
	v_add_f32_e32 v118, 1.0, v118
	v_rcp_f32_e32 v118, v118
	v_add_f32_e32 v119, 1.0, v119
	v_rcp_f32_e32 v119, v119
	v_add_f32_e32 v108, 1.0, v108
	v_mul_f32_e32 v118, v118, v120
	v_and_b32_e32 v120, 0xffff0000, v156
	v_mul_f32_e32 v119, v119, v120
	v_exp_f32_e32 v120, v116
	v_mul_f32_e32 v116, 0xbfb8aa3b, v117
	v_exp_f32_e32 v117, v116
	v_cvt_pk_bf16_f32 v116, v118, v119
	v_add_f32_e32 v118, 1.0, v120
	v_rcp_f32_e32 v118, v118
	v_add_f32_e32 v117, 1.0, v117
	v_rcp_f32_e32 v117, v117
	v_lshlrev_b32_e32 v119, 16, v157
	v_mul_f32_e32 v118, v118, v119
	v_and_b32_e32 v119, 0xffff0000, v157
	v_mul_f32_e32 v117, v117, v119
	v_cvt_pk_bf16_f32 v117, v118, v117
	global_store_dwordx4 v[122:123], v[114:117], off offset:256
	v_add_f32_e32 v109, 1.0, v109
	v_rcp_f32_e32 v113, v113
	v_or_b32_e32 v114, 16, v144
	v_ashrrev_i32_e32 v115, 31, v114
	v_lshlrev_b64 v[114:115], 10, v[114:115]
	v_lshl_add_u64 v[114:115], v[114:115], 0, v[142:143]
	v_lshlrev_b64 v[122:123], 1, v[114:115]
	v_lshl_add_u64 v[118:119], s[12:13], 0, v[122:123]
	s_mov_b32 s98, 0x800
	s_mov_b32 s99, 0
	v_lshl_add_u64 v[244:245], v[244:245], 0, s[98:99]
	global_load_dwordx4 v[114:117], v[244:245], off nt
	s_nop 0
; __device__ __forceinline__ unsigned pk2(float lo, float hi) { unsigned r; asm("v_cvt_pk_bf16_f32 %0, %1, %2" : "=v"(r) : "v"(lo), "v"(hi)); return r; }
; __device__ __forceinline__ float bflo(unsigned w) { return __uint_as_float(w << 16); }
; __device__ __forceinline__ float bfhi(unsigned w) { return __uint_as_float(w & 0xffff0000u); }
; __device__ __forceinline__ float sigmoidf_(float x) { return __builtin_amdgcn_rcpf(1.f + __expf(-x)); }
;     __device__ __forceinline__ void operator()(const f32x4 (&acc)[2][2][4][2], const Unit& u, int wr, int wc, int fr, int fq) const {
;         const int row0 = u.pm * 256 + wr * 64 + fr, col0 = u.pn * 256 + wc * 32 + 8 * fq;
; #pragma unroll
;         for (int ai = 0; ai < 2; ++ai)
; #pragma unroll
;             for (int m = 0; m < 4; ++m) { const size_t off = (size_t)(row0 + ai * 128 + m * 16) * D + col0;
; #pragma unroll
;                 for (int bj = 0; bj < 2; ++bj) { const v4u e = __builtin_nontemporal_load((const v4u*)(E + off + bj * 128)); const f32x4 v0 = acc[ai][bj][m][0], v1 = acc[ai][bj][m][1];
;                     v4u w; w.x = pk2(sigmoidf_(v0[0]) * bflo(e.x), sigmoidf_(v0[1]) * bfhi(e.x)); w.y = pk2(sigmoidf_(v0[2]) * bflo(e.y), sigmoidf_(v0[3]) * bfhi(e.y));
;                     w.z = pk2(sigmoidf_(v1[0]) * bflo(e.z), sigmoidf_(v1[1]) * bfhi(e.z)); w.w = pk2(sigmoidf_(v1[2]) * bflo(e.w), sigmoidf_(v1[3]) * bfhi(e.w));
;                     *(v4u*)(GE + off + bj * 128) = w; } }
	global_load_dwordx4 v[118:121], v[244:245], off offset:1024 nt
	v_rcp_f32_e32 v107, v107
	v_exp_f32_e32 v103, v103
	v_rcp_f32_e32 v106, v106
	v_rcp_f32_e32 v124, v108
	v_rcp_f32_e32 v109, v109
	v_add_f32_e32 v102, 1.0, v102
	v_rcp_f32_e32 v102, v102
	v_add_f32_e32 v103, 1.0, v103
	v_rcp_f32_e32 v103, v103
	v_mul_f32_e32 v104, 0xbfb8aa3b, v104
	v_exp_f32_e32 v104, v104
	v_mul_f32_e32 v105, 0xbfb8aa3b, v105
	v_exp_f32_e32 v105, v105
	v_mul_f32_e32 v98, 0xbfb8aa3b, v98
	v_exp_f32_e32 v98, v98
	v_mul_f32_e32 v99, 0xbfb8aa3b, v99
	v_exp_f32_e32 v99, v99
	v_mul_f32_e32 v100, 0xbfb8aa3b, v100
	v_add_f32_e32 v98, 1.0, v98
	v_rcp_f32_e32 v98, v98
	v_add_f32_e32 v99, 1.0, v99
	v_rcp_f32_e32 v99, v99
	v_exp_f32_e32 v100, v100
	v_mul_f32_e32 v101, 0xbfb8aa3b, v101
	v_exp_f32_e32 v101, v101
	v_mul_f32_e32 v94, 0xbfb8aa3b, v94
	v_mul_f32_e32 v95, 0xbfb8aa3b, v95
	v_exp_f32_e32 v94, v94
	v_exp_f32_e32 v95, v95
	v_mul_f32_e32 v96, 0xbfb8aa3b, v96
	v_mul_f32_e32 v97, 0xbfb8aa3b, v97
	v_add_f32_e32 v94, 1.0, v94
	v_add_f32_e32 v95, 1.0, v95
	v_rcp_f32_e32 v94, v94
	v_rcp_f32_e32 v95, v95
	v_exp_f32_e32 v96, v96
	v_exp_f32_e32 v97, v97
	v_mul_f32_e32 v90, 0xbfb8aa3b, v90
	v_exp_f32_e32 v90, v90
	v_mul_f32_e32 v91, 0xbfb8aa3b, v91
	v_exp_f32_e32 v91, v91
	v_mul_f32_e32 v92, 0xbfb8aa3b, v92
	v_add_f32_e32 v90, 1.0, v90
	v_rcp_f32_e32 v90, v90
	v_add_f32_e32 v91, 1.0, v91
	v_rcp_f32_e32 v91, v91
	v_exp_f32_e32 v92, v92
	v_mul_f32_e32 v93, 0xbfb8aa3b, v93
	v_exp_f32_e32 v93, v93
	v_mul_f32_e32 v86, 0xbfb8aa3b, v86
	v_exp_f32_e32 v86, v86
	v_mul_f32_e32 v87, 0xbfb8aa3b, v87
	v_exp_f32_e32 v87, v87
	v_mul_f32_e32 v88, 0xbfb8aa3b, v88
	v_add_f32_e32 v86, 1.0, v86
	v_rcp_f32_e32 v86, v86
	v_add_f32_e32 v87, 1.0, v87
	v_rcp_f32_e32 v87, v87
	v_exp_f32_e32 v88, v88
	v_mul_f32_e32 v89, 0xbfb8aa3b, v89
	v_exp_f32_e32 v89, v89
	v_mul_f32_e32 v82, 0xbfb8aa3b, v82
	v_exp_f32_e32 v82, v82
	v_mul_f32_e32 v83, 0xbfb8aa3b, v83
	v_exp_f32_e32 v83, v83
	v_mul_f32_e32 v84, 0xbfb8aa3b, v84
	v_add_f32_e32 v82, 1.0, v82
	v_rcp_f32_e32 v82, v82
	v_add_f32_e32 v83, 1.0, v83
	v_rcp_f32_e32 v83, v83
	v_exp_f32_e32 v84, v84
	v_mul_f32_e32 v85, 0xbfb8aa3b, v85
	v_exp_f32_e32 v85, v85
	v_mul_f32_e32 v78, 0xbfb8aa3b, v78
	v_mul_f32_e32 v79, 0xbfb8aa3b, v79
	v_exp_f32_e32 v78, v78
	v_exp_f32_e32 v79, v79
	v_mul_f32_e32 v80, 0xbfb8aa3b, v80
	s_waitcnt vmcnt(1)
	v_lshlrev_b32_e32 v108, 16, v114
	v_and_b32_e32 v114, 0xffff0000, v114
	v_lshlrev_b32_e32 v125, 16, v115
	v_and_b32_e32 v115, 0xffff0000, v115
	v_lshlrev_b32_e32 v126, 16, v116
	v_and_b32_e32 v116, 0xffff0000, v116
	v_mul_f32_e32 v108, v110, v108
	v_mul_f32_e32 v110, v111, v114
	v_mul_f32_e32 v111, v112, v125
	v_lshlrev_b32_e32 v127, 16, v117
	v_mul_f32_e32 v112, v113, v115
	v_mul_f32_e32 v114, v107, v116
	v_cvt_pk_bf16_f32 v107, v111, v112
	v_and_b32_e32 v111, 0xffff0000, v117
	v_mul_f32_e32 v113, v106, v126
	v_cvt_pk_bf16_f32 v106, v108, v110
	v_mul_f32_e32 v110, v124, v127
	v_mul_f32_e32 v109, v109, v111
	v_cvt_pk_bf16_f32 v109, v110, v109
	v_lshl_add_u64 v[110:111], s[6:7], 0, v[122:123]
	v_cvt_pk_bf16_f32 v108, v113, v114
	global_store_dwordx4 v[110:111], v[106:109], off
	v_add_f32_e32 v78, 1.0, v78
	v_add_f32_e32 v79, 1.0, v79
	s_waitcnt vmcnt(1)
	v_lshlrev_b32_e32 v106, 16, v118
	v_mul_f32_e32 v102, v102, v106
	v_and_b32_e32 v106, 0xffff0000, v118
	v_mul_f32_e32 v103, v103, v106
	v_cvt_pk_bf16_f32 v102, v102, v103
	v_add_f32_e32 v103, 1.0, v104
	v_rcp_f32_e32 v103, v103
	v_add_f32_e32 v104, 1.0, v105
	v_rcp_f32_e32 v104, v104
	v_lshlrev_b32_e32 v105, 16, v119
	v_mul_f32_e32 v103, v103, v105
	v_and_b32_e32 v105, 0xffff0000, v119
	v_mul_f32_e32 v104, v104, v105
	v_cvt_pk_bf16_f32 v103, v103, v104
	v_lshlrev_b32_e32 v104, 16, v120
	v_mul_f32_e32 v98, v98, v104
	v_and_b32_e32 v104, 0xffff0000, v120
	v_mul_f32_e32 v99, v99, v104
	v_cvt_pk_bf16_f32 v104, v98, v99
	v_add_f32_e32 v98, 1.0, v100
	v_rcp_f32_e32 v98, v98
	v_add_f32_e32 v99, 1.0, v101
	v_rcp_f32_e32 v99, v99
	v_lshlrev_b32_e32 v100, 16, v121
	v_mul_f32_e32 v98, v98, v100
	v_and_b32_e32 v100, 0xffff0000, v121
	v_mul_f32_e32 v99, v99, v100
	v_cvt_pk_bf16_f32 v105, v98, v99
	v_or_b32_e32 v98, 32, v144
	v_ashrrev_i32_e32 v99, 31, v98
	v_lshlrev_b64 v[98:99], 10, v[98:99]
	v_lshl_add_u64 v[98:99], v[98:99], 0, v[142:143]
	v_lshlrev_b64 v[106:107], 1, v[98:99]
	global_store_dwordx4 v[110:111], v[102:105], off offset:256
	v_rcp_f32_e32 v78, v78
	v_rcp_f32_e32 v79, v79
	v_lshl_add_u64 v[102:103], s[12:13], 0, v[106:107]
	s_mov_b32 s98, 0x800
	s_mov_b32 s99, 0
	v_lshl_add_u64 v[244:245], v[244:245], 0, s[98:99]
	global_load_dwordx4 v[98:101], v[244:245], off nt
	s_nop 0
	global_load_dwordx4 v[102:105], v[244:245], off offset:1024 nt
	v_exp_f32_e32 v80, v80
	v_mul_f32_e32 v81, 0xbfb8aa3b, v81
	v_exp_f32_e32 v81, v81
	v_mul_f32_e32 v74, 0xbfb8aa3b, v74
	v_exp_f32_e32 v74, v74
	v_mul_f32_e32 v75, 0xbfb8aa3b, v75
	v_exp_f32_e32 v75, v75
	v_mul_f32_e32 v76, 0xbfb8aa3b, v76
	v_add_f32_e32 v74, 1.0, v74
	v_rcp_f32_e32 v74, v74
	v_add_f32_e32 v75, 1.0, v75
	v_rcp_f32_e32 v75, v75
	v_exp_f32_e32 v76, v76
	v_mul_f32_e32 v77, 0xbfb8aa3b, v77
	v_exp_f32_e32 v77, v77
	v_mul_f32_e32 v70, 0xbfb8aa3b, v70
	v_exp_f32_e32 v70, v70
	v_mul_f32_e32 v71, 0xbfb8aa3b, v71
	v_exp_f32_e32 v71, v71
	v_mul_f32_e32 v72, 0xbfb8aa3b, v72
	v_add_f32_e32 v70, 1.0, v70
	v_rcp_f32_e32 v70, v70
	v_add_f32_e32 v71, 1.0, v71
	v_rcp_f32_e32 v71, v71
	v_exp_f32_e32 v72, v72
	v_mul_f32_e32 v73, 0xbfb8aa3b, v73
	v_exp_f32_e32 v73, v73
	v_mul_f32_e32 v66, 0xbfb8aa3b, v66
	v_exp_f32_e32 v66, v66
	v_mul_f32_e32 v67, 0xbfb8aa3b, v67
	v_exp_f32_e32 v67, v67
	v_mul_f32_e32 v68, 0xbfb8aa3b, v68
	v_add_f32_e32 v66, 1.0, v66
	v_rcp_f32_e32 v66, v66
	v_add_f32_e32 v67, 1.0, v67
	v_rcp_f32_e32 v67, v67
	v_exp_f32_e32 v68, v68
	v_mul_f32_e32 v69, 0xbfb8aa3b, v69
	v_exp_f32_e32 v69, v69
	s_mov_b64 s[4:5], 0x40000
	v_mul_f32_e32 v62, 0xbfb8aa3b, v62
	v_mul_f32_e32 v63, 0xbfb8aa3b, v63
	v_exp_f32_e32 v62, v62
	v_exp_f32_e32 v63, v63
	v_mul_f32_e32 v64, 0xbfb8aa3b, v64
	v_exp_f32_e32 v64, v64
	v_add_f32_e32 v62, 1.0, v62
	v_add_f32_e32 v63, 1.0, v63
	v_rcp_f32_e32 v62, v62
	v_rcp_f32_e32 v63, v63
	v_mul_f32_e32 v65, 0xbfb8aa3b, v65
	v_exp_f32_e32 v65, v65
	v_mul_f32_e32 v58, 0xbfb8aa3b, v58
	v_exp_f32_e32 v58, v58
	v_mul_f32_e32 v59, 0xbfb8aa3b, v59
	v_exp_f32_e32 v59, v59
	v_mul_f32_e32 v60, 0xbfb8aa3b, v60
	v_add_f32_e32 v58, 1.0, v58
	v_rcp_f32_e32 v58, v58
	v_add_f32_e32 v59, 1.0, v59
	v_rcp_f32_e32 v59, v59
	v_exp_f32_e32 v60, v60
	v_mul_f32_e32 v61, 0xbfb8aa3b, v61
	v_exp_f32_e32 v61, v61
	v_mul_f32_e32 v54, 0xbfb8aa3b, v54
	v_exp_f32_e32 v54, v54
	v_mul_f32_e32 v55, 0xbfb8aa3b, v55
	v_exp_f32_e32 v55, v55
	v_mul_f32_e32 v56, 0xbfb8aa3b, v56
	v_add_f32_e32 v54, 1.0, v54
	v_rcp_f32_e32 v54, v54
	v_add_f32_e32 v55, 1.0, v55
	v_rcp_f32_e32 v55, v55
	v_exp_f32_e32 v56, v56
	v_mul_f32_e32 v57, 0xbfb8aa3b, v57
	v_exp_f32_e32 v57, v57
	v_mul_f32_e32 v50, 0xbfb8aa3b, v50
	v_exp_f32_e32 v50, v50
	s_waitcnt vmcnt(1)
; __device__ __forceinline__ unsigned pk2(float lo, float hi) { unsigned r; asm("v_cvt_pk_bf16_f32 %0, %1, %2" : "=v"(r) : "v"(lo), "v"(hi)); return r; }
; __device__ __forceinline__ float bflo(unsigned w) { return __uint_as_float(w << 16); }
; __device__ __forceinline__ float bfhi(unsigned w) { return __uint_as_float(w & 0xffff0000u); }
; __device__ __forceinline__ float sigmoidf_(float x) { return __builtin_amdgcn_rcpf(1.f + __expf(-x)); }
;     __device__ __forceinline__ void operator()(const f32x4 (&acc)[2][2][4][2], const Unit& u, int wr, int wc, int fr, int fq) const {
;         const int row0 = u.pm * 256 + wr * 64 + fr, col0 = u.pn * 256 + wc * 32 + 8 * fq;
; #pragma unroll
;         for (int ai = 0; ai < 2; ++ai)
; #pragma unroll
;             for (int m = 0; m < 4; ++m) { const size_t off = (size_t)(row0 + ai * 128 + m * 16) * D + col0;
; #pragma unroll
;                 for (int bj = 0; bj < 2; ++bj) { const v4u e = __builtin_nontemporal_load((const v4u*)(E + off + bj * 128)); const f32x4 v0 = acc[ai][bj][m][0], v1 = acc[ai][bj][m][1];
;                     v4u w; w.x = pk2(sigmoidf_(v0[0]) * bflo(e.x), sigmoidf_(v0[1]) * bfhi(e.x)); w.y = pk2(sigmoidf_(v0[2]) * bflo(e.y), sigmoidf_(v0[3]) * bfhi(e.y));
;                     w.z = pk2(sigmoidf_(v1[0]) * bflo(e.z), sigmoidf_(v1[1]) * bfhi(e.z)); w.w = pk2(sigmoidf_(v1[2]) * bflo(e.w), sigmoidf_(v1[3]) * bfhi(e.w));
;                     *(v4u*)(GE + off + bj * 128) = w; } }
	v_lshlrev_b32_e32 v108, 16, v98
	v_and_b32_e32 v98, 0xffff0000, v98
	v_mul_f32_e32 v94, v94, v108
	v_mul_f32_e32 v95, v95, v98
	v_cvt_pk_bf16_f32 v94, v94, v95
	v_add_f32_e32 v95, 1.0, v96
	v_rcp_f32_e32 v95, v95
	v_add_f32_e32 v96, 1.0, v97
	v_rcp_f32_e32 v96, v96
	v_lshlrev_b32_e32 v97, 16, v99
	v_mul_f32_e32 v95, v95, v97
	v_and_b32_e32 v97, 0xffff0000, v99
	v_mul_f32_e32 v96, v96, v97
	v_cvt_pk_bf16_f32 v95, v95, v96
	v_lshlrev_b32_e32 v96, 16, v100
	v_mul_f32_e32 v90, v90, v96
	v_and_b32_e32 v96, 0xffff0000, v100
	v_mul_f32_e32 v91, v91, v96
	v_cvt_pk_bf16_f32 v96, v90, v91
	v_add_f32_e32 v90, 1.0, v92
	v_rcp_f32_e32 v90, v90
	v_add_f32_e32 v91, 1.0, v93
	v_rcp_f32_e32 v91, v91
	v_lshlrev_b32_e32 v92, 16, v101
	v_mul_f32_e32 v90, v90, v92
	v_and_b32_e32 v92, 0xffff0000, v101
	v_mul_f32_e32 v91, v91, v92
	s_waitcnt vmcnt(0)
	v_lshlrev_b32_e32 v92, 16, v102
	v_mul_f32_e32 v86, v86, v92
	v_and_b32_e32 v92, 0xffff0000, v102
	v_mul_f32_e32 v87, v87, v92
	v_cvt_pk_bf16_f32 v86, v86, v87
	v_add_f32_e32 v87, 1.0, v88
	v_rcp_f32_e32 v87, v87
	v_add_f32_e32 v88, 1.0, v89
	v_rcp_f32_e32 v88, v88
	v_lshlrev_b32_e32 v89, 16, v103
	v_mul_f32_e32 v87, v87, v89
	v_and_b32_e32 v89, 0xffff0000, v103
	v_mul_f32_e32 v88, v88, v89
	v_cvt_pk_bf16_f32 v87, v87, v88
	v_lshlrev_b32_e32 v88, 16, v104
	v_mul_f32_e32 v82, v82, v88
	v_and_b32_e32 v88, 0xffff0000, v104
	v_mul_f32_e32 v83, v83, v88
	v_cvt_pk_bf16_f32 v88, v82, v83
	v_add_f32_e32 v82, 1.0, v84
	v_rcp_f32_e32 v82, v82
	v_add_f32_e32 v83, 1.0, v85
	v_rcp_f32_e32 v83, v83
	v_lshlrev_b32_e32 v84, 16, v105
	v_mul_f32_e32 v82, v82, v84
	v_and_b32_e32 v84, 0xffff0000, v105
	v_mul_f32_e32 v83, v83, v84
	v_cvt_pk_bf16_f32 v89, v82, v83
	v_or_b32_e32 v82, 48, v144
	v_ashrrev_i32_e32 v83, 31, v82
	v_lshlrev_b64 v[82:83], 10, v[82:83]
	v_cvt_pk_bf16_f32 v97, v90, v91
	v_lshl_add_u64 v[90:91], s[6:7], 0, v[106:107]
	v_lshl_add_u64 v[82:83], v[82:83], 0, v[142:143]
	global_store_dwordx4 v[90:91], v[94:97], off
	global_store_dwordx4 v[90:91], v[86:89], off offset:256
	v_lshlrev_b64 v[90:91], 1, v[82:83]
	v_mul_f32_e32 v51, 0xbfb8aa3b, v51
	v_lshl_add_u64 v[86:87], s[12:13], 0, v[90:91]
	s_mov_b32 s98, 0x800
	s_mov_b32 s99, 0
	v_lshl_add_u64 v[244:245], v[244:245], 0, s[98:99]
	global_load_dwordx4 v[82:85], v[244:245], off nt
	s_nop 0
	global_load_dwordx4 v[86:89], v[244:245], off offset:1024 nt
	v_exp_f32_e32 v51, v51
	v_add_f32_e32 v50, 1.0, v50
	v_rcp_f32_e32 v50, v50
	v_mul_f32_e32 v52, 0xbfb8aa3b, v52
	v_add_f32_e32 v51, 1.0, v51
	v_rcp_f32_e32 v51, v51
	v_exp_f32_e32 v52, v52
	v_mul_f32_e32 v53, 0xbfb8aa3b, v53
	v_exp_f32_e32 v53, v53
	v_mul_f32_e32 v46, 0xbfb8aa3b, v46
	v_mul_f32_e32 v47, 0xbfb8aa3b, v47
	v_exp_f32_e32 v46, v46
	v_exp_f32_e32 v47, v47
	v_mul_f32_e32 v48, 0xbfb8aa3b, v48
	v_exp_f32_e32 v48, v48
	v_add_f32_e32 v46, 1.0, v46
	v_add_f32_e32 v47, 1.0, v47
	v_rcp_f32_e32 v46, v46
	v_rcp_f32_e32 v47, v47
	v_mul_f32_e32 v49, 0xbfb8aa3b, v49
	v_exp_f32_e32 v49, v49
	v_mul_f32_e32 v42, 0xbfb8aa3b, v42
	v_exp_f32_e32 v42, v42
	v_mul_f32_e32 v43, 0xbfb8aa3b, v43
	v_exp_f32_e32 v43, v43
	v_mul_f32_e32 v44, 0xbfb8aa3b, v44
	v_add_f32_e32 v42, 1.0, v42
	v_rcp_f32_e32 v42, v42
	v_add_f32_e32 v43, 1.0, v43
	v_rcp_f32_e32 v43, v43
	v_exp_f32_e32 v44, v44
	v_mul_f32_e32 v45, 0xbfb8aa3b, v45
	v_exp_f32_e32 v45, v45
	v_mul_f32_e32 v38, 0xbfb8aa3b, v38
	v_exp_f32_e32 v38, v38
	v_mul_f32_e32 v39, 0xbfb8aa3b, v39
	v_exp_f32_e32 v39, v39
	v_mul_f32_e32 v40, 0xbfb8aa3b, v40
	v_add_f32_e32 v38, 1.0, v38
	v_rcp_f32_e32 v38, v38
	v_add_f32_e32 v39, 1.0, v39
	v_rcp_f32_e32 v39, v39
	v_exp_f32_e32 v40, v40
	v_mul_f32_e32 v41, 0xbfb8aa3b, v41
	v_exp_f32_e32 v41, v41
	v_mul_f32_e32 v34, 0xbfb8aa3b, v34
	v_exp_f32_e32 v34, v34
	v_mul_f32_e32 v35, 0xbfb8aa3b, v35
	v_exp_f32_e32 v35, v35
	v_mul_f32_e32 v36, 0xbfb8aa3b, v36
	v_add_f32_e32 v34, 1.0, v34
	v_rcp_f32_e32 v34, v34
	v_add_f32_e32 v35, 1.0, v35
	v_rcp_f32_e32 v35, v35
	v_exp_f32_e32 v36, v36
	v_mul_f32_e32 v37, 0xbfb8aa3b, v37
	v_exp_f32_e32 v37, v37
	v_mul_f32_e32 v30, 0xbfb8aa3b, v30
	v_mul_f32_e32 v31, 0xbfb8aa3b, v31
	v_exp_f32_e32 v30, v30
	v_exp_f32_e32 v31, v31
	v_mul_f32_e32 v32, 0xbfb8aa3b, v32
	v_exp_f32_e32 v32, v32
	v_add_f32_e32 v30, 1.0, v30
	v_add_f32_e32 v31, 1.0, v31
	v_rcp_f32_e32 v30, v30
	v_rcp_f32_e32 v31, v31
	v_mul_f32_e32 v33, 0xbfb8aa3b, v33
	v_exp_f32_e32 v33, v33
	v_mul_f32_e32 v26, 0xbfb8aa3b, v26
	v_exp_f32_e32 v26, v26
	v_mul_f32_e32 v27, 0xbfb8aa3b, v27
	v_exp_f32_e32 v27, v27
	v_mul_f32_e32 v28, 0xbfb8aa3b, v28
	v_add_f32_e32 v26, 1.0, v26
	v_rcp_f32_e32 v26, v26
	v_add_f32_e32 v27, 1.0, v27
	v_rcp_f32_e32 v27, v27
	s_waitcnt vmcnt(1)
	v_lshlrev_b32_e32 v92, 16, v82
	v_and_b32_e32 v82, 0xffff0000, v82
	v_mul_f32_e32 v78, v78, v92
	v_mul_f32_e32 v79, v79, v82
	v_cvt_pk_bf16_f32 v78, v78, v79
	v_add_f32_e32 v79, 1.0, v80
	v_rcp_f32_e32 v79, v79
	v_add_f32_e32 v80, 1.0, v81
	v_rcp_f32_e32 v80, v80
	v_lshlrev_b32_e32 v81, 16, v83
	v_mul_f32_e32 v79, v79, v81
	v_and_b32_e32 v81, 0xffff0000, v83
	v_mul_f32_e32 v80, v80, v81
	v_cvt_pk_bf16_f32 v79, v79, v80
	v_lshlrev_b32_e32 v80, 16, v84
	v_mul_f32_e32 v74, v74, v80
	v_and_b32_e32 v80, 0xffff0000, v84
	v_mul_f32_e32 v75, v75, v80
	v_cvt_pk_bf16_f32 v80, v74, v75
	v_add_f32_e32 v74, 1.0, v76
	v_rcp_f32_e32 v74, v74
	v_add_f32_e32 v75, 1.0, v77
	v_rcp_f32_e32 v75, v75
	v_lshlrev_b32_e32 v76, 16, v85
	v_mul_f32_e32 v74, v74, v76
	v_and_b32_e32 v76, 0xffff0000, v85
	v_mul_f32_e32 v75, v75, v76
	s_waitcnt vmcnt(0)
; __device__ __forceinline__ unsigned pk2(float lo, float hi) { unsigned r; asm("v_cvt_pk_bf16_f32 %0, %1, %2" : "=v"(r) : "v"(lo), "v"(hi)); return r; }
; __device__ __forceinline__ float bflo(unsigned w) { return __uint_as_float(w << 16); }
; __device__ __forceinline__ float bfhi(unsigned w) { return __uint_as_float(w & 0xffff0000u); }
; __device__ __forceinline__ float sigmoidf_(float x) { return __builtin_amdgcn_rcpf(1.f + __expf(-x)); }
;     __device__ __forceinline__ void operator()(const f32x4 (&acc)[2][2][4][2], const Unit& u, int wr, int wc, int fr, int fq) const {
;         const int row0 = u.pm * 256 + wr * 64 + fr, col0 = u.pn * 256 + wc * 32 + 8 * fq;
; #pragma unroll
;         for (int ai = 0; ai < 2; ++ai)
; #pragma unroll
;             for (int m = 0; m < 4; ++m) { const size_t off = (size_t)(row0 + ai * 128 + m * 16) * D + col0;
; #pragma unroll
;                 for (int bj = 0; bj < 2; ++bj) { const v4u e = __builtin_nontemporal_load((const v4u*)(E + off + bj * 128)); const f32x4 v0 = acc[ai][bj][m][0], v1 = acc[ai][bj][m][1];
;                     v4u w; w.x = pk2(sigmoidf_(v0[0]) * bflo(e.x), sigmoidf_(v0[1]) * bfhi(e.x)); w.y = pk2(sigmoidf_(v0[2]) * bflo(e.y), sigmoidf_(v0[3]) * bfhi(e.y));
;                     w.z = pk2(sigmoidf_(v1[0]) * bflo(e.z), sigmoidf_(v1[1]) * bfhi(e.z)); w.w = pk2(sigmoidf_(v1[2]) * bflo(e.w), sigmoidf_(v1[3]) * bfhi(e.w));
;                     *(v4u*)(GE + off + bj * 128) = w; } }
	v_lshlrev_b32_e32 v76, 16, v86
	v_mul_f32_e32 v70, v70, v76
	v_and_b32_e32 v76, 0xffff0000, v86
	v_mul_f32_e32 v71, v71, v76
	v_cvt_pk_bf16_f32 v70, v70, v71
	v_add_f32_e32 v71, 1.0, v72
	v_rcp_f32_e32 v71, v71
	v_add_f32_e32 v72, 1.0, v73
	v_rcp_f32_e32 v72, v72
	v_lshlrev_b32_e32 v73, 16, v87
	v_mul_f32_e32 v71, v71, v73
	v_and_b32_e32 v73, 0xffff0000, v87
	v_mul_f32_e32 v72, v72, v73
	v_cvt_pk_bf16_f32 v71, v71, v72
	v_lshlrev_b32_e32 v72, 16, v88
	v_mul_f32_e32 v66, v66, v72
	v_and_b32_e32 v72, 0xffff0000, v88
	v_mul_f32_e32 v67, v67, v72
	v_cvt_pk_bf16_f32 v72, v66, v67
	v_add_f32_e32 v66, 1.0, v68
	v_rcp_f32_e32 v66, v66
	v_add_f32_e32 v67, 1.0, v69
	v_rcp_f32_e32 v67, v67
	v_lshlrev_b32_e32 v68, 16, v89
	v_cvt_pk_bf16_f32 v81, v74, v75
	v_lshl_add_u64 v[74:75], s[6:7], 0, v[90:91]
	v_mul_f32_e32 v66, v66, v68
	v_and_b32_e32 v68, 0xffff0000, v89
	global_store_dwordx4 v[74:75], v[78:81], off
	v_mul_f32_e32 v67, v67, v68
	v_cvt_pk_bf16_f32 v73, v66, v67
	global_store_dwordx4 v[74:75], v[70:73], off offset:256
	v_lshl_add_u64 v[74:75], v[140:141], 0, s[4:5]
	s_mov_b64 s[4:5], 0x48000
	v_lshl_add_u64 v[70:71], s[12:13], 0, v[74:75]
	s_mov_b32 s98, 0x800
	s_mov_b32 s99, 0
	v_lshl_add_u64 v[244:245], v[244:245], 0, s[98:99]
	global_load_dwordx4 v[66:69], v[244:245], off nt
	s_nop 0
	global_load_dwordx4 v[70:73], v[244:245], off offset:1024 nt
	v_exp_f32_e32 v28, v28
	v_mul_f32_e32 v29, 0xbfb8aa3b, v29
	v_exp_f32_e32 v29, v29
	v_mul_f32_e32 v22, 0xbfb8aa3b, v22
	v_exp_f32_e32 v22, v22
	v_mul_f32_e32 v23, 0xbfb8aa3b, v23
	v_exp_f32_e32 v23, v23
	v_mul_f32_e32 v24, 0xbfb8aa3b, v24
	v_add_f32_e32 v22, 1.0, v22
	v_rcp_f32_e32 v22, v22
	v_add_f32_e32 v23, 1.0, v23
	v_rcp_f32_e32 v23, v23
	v_exp_f32_e32 v24, v24
	v_mul_f32_e32 v25, 0xbfb8aa3b, v25
	v_exp_f32_e32 v25, v25
	v_mul_f32_e32 v18, 0xbfb8aa3b, v18
	v_exp_f32_e32 v18, v18
	v_mul_f32_e32 v19, 0xbfb8aa3b, v19
	v_exp_f32_e32 v19, v19
	v_mul_f32_e32 v20, 0xbfb8aa3b, v20
	v_add_f32_e32 v18, 1.0, v18
	v_rcp_f32_e32 v18, v18
	v_add_f32_e32 v19, 1.0, v19
	v_rcp_f32_e32 v19, v19
	v_exp_f32_e32 v20, v20
	v_mul_f32_e32 v21, 0xbfb8aa3b, v21
	v_exp_f32_e32 v21, v21
	v_mul_f32_e32 v14, 0xbfb8aa3b, v14
	v_mul_f32_e32 v15, 0xbfb8aa3b, v15
	v_exp_f32_e32 v14, v14
	v_exp_f32_e32 v15, v15
	v_mul_f32_e32 v16, 0xbfb8aa3b, v16
	v_exp_f32_e32 v16, v16
	v_add_f32_e32 v14, 1.0, v14
	v_add_f32_e32 v15, 1.0, v15
	v_rcp_f32_e32 v14, v14
	v_rcp_f32_e32 v15, v15
	v_mul_f32_e32 v17, 0xbfb8aa3b, v17
	v_exp_f32_e32 v17, v17
	v_mul_f32_e32 v10, 0xbfb8aa3b, v10
	v_exp_f32_e32 v10, v10
	v_mul_f32_e32 v11, 0xbfb8aa3b, v11
	v_exp_f32_e32 v11, v11
	v_mul_f32_e32 v12, 0xbfb8aa3b, v12
	v_add_f32_e32 v10, 1.0, v10
	v_rcp_f32_e32 v10, v10
	v_add_f32_e32 v11, 1.0, v11
	v_rcp_f32_e32 v11, v11
	v_exp_f32_e32 v12, v12
	v_mul_f32_e32 v13, 0xbfb8aa3b, v13
	v_exp_f32_e32 v13, v13
	v_mul_f32_e32 v6, 0xbfb8aa3b, v6
	v_exp_f32_e32 v6, v6
	v_mul_f32_e32 v7, 0xbfb8aa3b, v7
	v_exp_f32_e32 v7, v7
	v_mul_f32_e32 v8, 0xbfb8aa3b, v8
	v_add_f32_e32 v6, 1.0, v6
	v_rcp_f32_e32 v6, v6
	v_add_f32_e32 v7, 1.0, v7
	v_rcp_f32_e32 v7, v7
	v_exp_f32_e32 v8, v8
	v_mul_f32_e32 v9, 0xbfb8aa3b, v9
	v_exp_f32_e32 v9, v9
	v_mul_f32_e32 v2, 0xbfb8aa3b, v2
	v_exp_f32_e32 v2, v2
	v_mul_f32_e32 v3, 0xbfb8aa3b, v3
	v_exp_f32_e32 v3, v3
	v_mul_f32_e32 v4, 0xbfb8aa3b, v4
	v_add_f32_e32 v2, 1.0, v2
	v_rcp_f32_e32 v2, v2
	v_add_f32_e32 v3, 1.0, v3
	v_rcp_f32_e32 v3, v3
	v_exp_f32_e32 v4, v4
	v_mul_f32_e32 v5, 0xbfb8aa3b, v5
	v_exp_f32_e32 v5, v5
	s_andn2_b64 vcc, exec, s[38:39]
	s_mov_b64 s[8:9], -1
	s_mov_b32 s25, 0x38600000
	s_waitcnt vmcnt(1)
	v_lshlrev_b32_e32 v76, 16, v66
	v_and_b32_e32 v66, 0xffff0000, v66
	v_mul_f32_e32 v62, v62, v76
	v_mul_f32_e32 v63, v63, v66
	v_cvt_pk_bf16_f32 v62, v62, v63
	v_add_f32_e32 v63, 1.0, v64
	v_rcp_f32_e32 v63, v63
	v_add_f32_e32 v64, 1.0, v65
	v_rcp_f32_e32 v64, v64
	v_lshlrev_b32_e32 v65, 16, v67
	v_mul_f32_e32 v63, v63, v65
	v_and_b32_e32 v65, 0xffff0000, v67
	v_mul_f32_e32 v64, v64, v65
	v_cvt_pk_bf16_f32 v63, v63, v64
	v_lshlrev_b32_e32 v64, 16, v68
	v_mul_f32_e32 v58, v58, v64
	v_and_b32_e32 v64, 0xffff0000, v68
	v_mul_f32_e32 v59, v59, v64
	v_cvt_pk_bf16_f32 v64, v58, v59
	v_add_f32_e32 v58, 1.0, v60
	v_rcp_f32_e32 v58, v58
	v_add_f32_e32 v59, 1.0, v61
	v_rcp_f32_e32 v59, v59
	v_lshlrev_b32_e32 v60, 16, v69
	v_mul_f32_e32 v58, v58, v60
	v_and_b32_e32 v60, 0xffff0000, v69
	v_mul_f32_e32 v59, v59, v60
	s_waitcnt vmcnt(0)
	v_lshlrev_b32_e32 v60, 16, v70
	v_mul_f32_e32 v54, v54, v60
	v_and_b32_e32 v60, 0xffff0000, v70
	v_mul_f32_e32 v55, v55, v60
	v_cvt_pk_bf16_f32 v54, v54, v55
	v_add_f32_e32 v55, 1.0, v56
	v_rcp_f32_e32 v55, v55
	v_add_f32_e32 v56, 1.0, v57
	v_rcp_f32_e32 v56, v56
	v_lshlrev_b32_e32 v57, 16, v71
	v_mul_f32_e32 v55, v55, v57
	v_and_b32_e32 v57, 0xffff0000, v71
	v_mul_f32_e32 v56, v56, v57
	v_cvt_pk_bf16_f32 v55, v55, v56
	v_lshlrev_b32_e32 v56, 16, v72
	v_mul_f32_e32 v50, v50, v56
	v_and_b32_e32 v56, 0xffff0000, v72
	v_mul_f32_e32 v51, v51, v56
	v_cvt_pk_bf16_f32 v56, v50, v51
	v_add_f32_e32 v50, 1.0, v52
	v_rcp_f32_e32 v50, v50
	v_add_f32_e32 v51, 1.0, v53
	v_rcp_f32_e32 v51, v51
	v_lshlrev_b32_e32 v52, 16, v73
	v_cvt_pk_bf16_f32 v65, v58, v59
	v_lshl_add_u64 v[58:59], s[6:7], 0, v[74:75]
	v_mul_f32_e32 v50, v50, v52
	v_and_b32_e32 v52, 0xffff0000, v73
	global_store_dwordx4 v[58:59], v[62:65], off
	v_mul_f32_e32 v51, v51, v52
	v_cvt_pk_bf16_f32 v57, v50, v51
	global_store_dwordx4 v[58:59], v[54:57], off offset:256
	v_lshl_add_u64 v[58:59], v[140:141], 0, s[4:5]
	s_mov_b64 s[4:5], 0x50000
	v_lshl_add_u64 v[54:55], s[12:13], 0, v[58:59]
	s_mov_b32 s98, 0x800
	s_mov_b32 s99, 0
	v_lshl_add_u64 v[244:245], v[244:245], 0, s[98:99]
	global_load_dwordx4 v[50:53], v[244:245], off nt
	s_nop 0
	global_load_dwordx4 v[54:57], v[244:245], off offset:1024 nt
	s_waitcnt vmcnt(1)
; __device__ __forceinline__ unsigned pk2(float lo, float hi) { unsigned r; asm("v_cvt_pk_bf16_f32 %0, %1, %2" : "=v"(r) : "v"(lo), "v"(hi)); return r; }
; __device__ __forceinline__ float bflo(unsigned w) { return __uint_as_float(w << 16); }
; __device__ __forceinline__ float bfhi(unsigned w) { return __uint_as_float(w & 0xffff0000u); }
; __device__ __forceinline__ float sigmoidf_(float x) { return __builtin_amdgcn_rcpf(1.f + __expf(-x)); }
;     __device__ __forceinline__ void operator()(const f32x4 (&acc)[2][2][4][2], const Unit& u, int wr, int wc, int fr, int fq) const {
;         const int row0 = u.pm * 256 + wr * 64 + fr, col0 = u.pn * 256 + wc * 32 + 8 * fq;
; #pragma unroll
;         for (int ai = 0; ai < 2; ++ai)
; #pragma unroll
;             for (int m = 0; m < 4; ++m) { const size_t off = (size_t)(row0 + ai * 128 + m * 16) * D + col0;
; #pragma unroll
;                 for (int bj = 0; bj < 2; ++bj) { const v4u e = __builtin_nontemporal_load((const v4u*)(E + off + bj * 128)); const f32x4 v0 = acc[ai][bj][m][0], v1 = acc[ai][bj][m][1];
;                     v4u w; w.x = pk2(sigmoidf_(v0[0]) * bflo(e.x), sigmoidf_(v0[1]) * bfhi(e.x)); w.y = pk2(sigmoidf_(v0[2]) * bflo(e.y), sigmoidf_(v0[3]) * bfhi(e.y));
;                     w.z = pk2(sigmoidf_(v1[0]) * bflo(e.z), sigmoidf_(v1[1]) * bfhi(e.z)); w.w = pk2(sigmoidf_(v1[2]) * bflo(e.w), sigmoidf_(v1[3]) * bfhi(e.w));
;                     *(v4u*)(GE + off + bj * 128) = w; } }
	v_lshlrev_b32_e32 v60, 16, v50
	v_and_b32_e32 v50, 0xffff0000, v50
	v_mul_f32_e32 v46, v46, v60
	v_mul_f32_e32 v47, v47, v50
	v_cvt_pk_bf16_f32 v46, v46, v47
	v_add_f32_e32 v47, 1.0, v48
	v_rcp_f32_e32 v47, v47
	v_add_f32_e32 v48, 1.0, v49
	v_rcp_f32_e32 v48, v48
	v_lshlrev_b32_e32 v49, 16, v51
	v_mul_f32_e32 v47, v47, v49
	v_and_b32_e32 v49, 0xffff0000, v51
	v_mul_f32_e32 v48, v48, v49
	v_cvt_pk_bf16_f32 v47, v47, v48
	v_lshlrev_b32_e32 v48, 16, v52
	v_mul_f32_e32 v42, v42, v48
	v_and_b32_e32 v48, 0xffff0000, v52
	v_mul_f32_e32 v43, v43, v48
	v_cvt_pk_bf16_f32 v48, v42, v43
	v_add_f32_e32 v42, 1.0, v44
	v_rcp_f32_e32 v42, v42
	v_add_f32_e32 v43, 1.0, v45
	v_rcp_f32_e32 v43, v43
	v_lshlrev_b32_e32 v44, 16, v53
	v_mul_f32_e32 v42, v42, v44
	v_and_b32_e32 v44, 0xffff0000, v53
	v_mul_f32_e32 v43, v43, v44
	s_waitcnt vmcnt(0)
	v_lshlrev_b32_e32 v44, 16, v54
	v_mul_f32_e32 v38, v38, v44
	v_and_b32_e32 v44, 0xffff0000, v54
	v_mul_f32_e32 v39, v39, v44
	v_cvt_pk_bf16_f32 v38, v38, v39
	v_add_f32_e32 v39, 1.0, v40
	v_rcp_f32_e32 v39, v39
	v_add_f32_e32 v40, 1.0, v41
	v_rcp_f32_e32 v40, v40
	v_lshlrev_b32_e32 v41, 16, v55
	v_mul_f32_e32 v39, v39, v41
	v_and_b32_e32 v41, 0xffff0000, v55
	v_mul_f32_e32 v40, v40, v41
	v_cvt_pk_bf16_f32 v39, v39, v40
	v_lshlrev_b32_e32 v40, 16, v56
	v_mul_f32_e32 v34, v34, v40
	v_and_b32_e32 v40, 0xffff0000, v56
	v_mul_f32_e32 v35, v35, v40
	v_cvt_pk_bf16_f32 v40, v34, v35
	v_add_f32_e32 v34, 1.0, v36
	v_rcp_f32_e32 v34, v34
	v_add_f32_e32 v35, 1.0, v37
	v_rcp_f32_e32 v35, v35
	v_lshlrev_b32_e32 v36, 16, v57
	v_cvt_pk_bf16_f32 v49, v42, v43
	v_lshl_add_u64 v[42:43], s[6:7], 0, v[58:59]
	v_mul_f32_e32 v34, v34, v36
	v_and_b32_e32 v36, 0xffff0000, v57
	global_store_dwordx4 v[42:43], v[46:49], off
	v_mul_f32_e32 v35, v35, v36
	v_cvt_pk_bf16_f32 v41, v34, v35
	global_store_dwordx4 v[42:43], v[38:41], off offset:256
	v_lshl_add_u64 v[42:43], v[140:141], 0, s[4:5]
	s_mov_b64 s[4:5], 0x58000
	v_lshl_add_u64 v[38:39], s[12:13], 0, v[42:43]
	s_mov_b32 s98, 0x800
	s_mov_b32 s99, 0
	v_lshl_add_u64 v[244:245], v[244:245], 0, s[98:99]
	global_load_dwordx4 v[34:37], v[244:245], off nt
	s_nop 0
	global_load_dwordx4 v[38:41], v[244:245], off offset:1024 nt
	s_waitcnt vmcnt(1)
	v_lshlrev_b32_e32 v44, 16, v34
	v_and_b32_e32 v34, 0xffff0000, v34
	v_mul_f32_e32 v30, v30, v44
	v_mul_f32_e32 v31, v31, v34
	v_cvt_pk_bf16_f32 v30, v30, v31
	v_add_f32_e32 v31, 1.0, v32
	v_rcp_f32_e32 v31, v31
	v_add_f32_e32 v32, 1.0, v33
	v_rcp_f32_e32 v32, v32
	v_lshlrev_b32_e32 v33, 16, v35
	v_mul_f32_e32 v31, v31, v33
	v_and_b32_e32 v33, 0xffff0000, v35
	v_mul_f32_e32 v32, v32, v33
	v_cvt_pk_bf16_f32 v31, v31, v32
	v_lshlrev_b32_e32 v32, 16, v36
	v_mul_f32_e32 v26, v26, v32
	v_and_b32_e32 v32, 0xffff0000, v36
	v_mul_f32_e32 v27, v27, v32
	v_cvt_pk_bf16_f32 v32, v26, v27
	v_add_f32_e32 v26, 1.0, v28
	v_rcp_f32_e32 v26, v26
	v_add_f32_e32 v27, 1.0, v29
	v_rcp_f32_e32 v27, v27
	v_lshlrev_b32_e32 v28, 16, v37
	v_mul_f32_e32 v26, v26, v28
	v_and_b32_e32 v28, 0xffff0000, v37
	v_mul_f32_e32 v27, v27, v28
	s_waitcnt vmcnt(0)
	v_lshlrev_b32_e32 v28, 16, v38
	v_mul_f32_e32 v22, v22, v28
	v_and_b32_e32 v28, 0xffff0000, v38
	v_mul_f32_e32 v23, v23, v28
	v_cvt_pk_bf16_f32 v22, v22, v23
	v_add_f32_e32 v23, 1.0, v24
	v_rcp_f32_e32 v23, v23
	v_add_f32_e32 v24, 1.0, v25
	v_rcp_f32_e32 v24, v24
	v_lshlrev_b32_e32 v25, 16, v39
	v_mul_f32_e32 v23, v23, v25
	v_and_b32_e32 v25, 0xffff0000, v39
	v_mul_f32_e32 v24, v24, v25
	v_cvt_pk_bf16_f32 v23, v23, v24
	v_lshlrev_b32_e32 v24, 16, v40
	v_mul_f32_e32 v18, v18, v24
	v_and_b32_e32 v24, 0xffff0000, v40
	v_mul_f32_e32 v19, v19, v24
	v_cvt_pk_bf16_f32 v24, v18, v19
	v_add_f32_e32 v18, 1.0, v20
	v_rcp_f32_e32 v18, v18
	v_add_f32_e32 v19, 1.0, v21
	v_rcp_f32_e32 v19, v19
	v_lshlrev_b32_e32 v20, 16, v41
	v_cvt_pk_bf16_f32 v33, v26, v27
	v_lshl_add_u64 v[26:27], s[6:7], 0, v[42:43]
	v_mul_f32_e32 v18, v18, v20
	v_and_b32_e32 v20, 0xffff0000, v41
	global_store_dwordx4 v[26:27], v[30:33], off
	v_mul_f32_e32 v19, v19, v20
	v_cvt_pk_bf16_f32 v25, v18, v19
	global_store_dwordx4 v[26:27], v[22:25], off offset:256
	v_lshl_add_u64 v[26:27], v[140:141], 0, s[4:5]
	s_nop 0
	v_lshl_add_u64 v[22:23], s[12:13], 0, v[26:27]
	s_mov_b32 s98, 0x800
	s_mov_b32 s99, 0
	v_lshl_add_u64 v[244:245], v[244:245], 0, s[98:99]
	global_load_dwordx4 v[18:21], v[244:245], off nt
	s_nop 0
	global_load_dwordx4 v[22:25], v[244:245], off offset:1024 nt
	s_waitcnt vmcnt(1)
	v_lshlrev_b32_e32 v28, 16, v18
	v_and_b32_e32 v18, 0xffff0000, v18
	v_mul_f32_e32 v14, v14, v28
	v_mul_f32_e32 v15, v15, v18
	v_cvt_pk_bf16_f32 v14, v14, v15
	v_add_f32_e32 v15, 1.0, v16
	v_rcp_f32_e32 v15, v15
	v_add_f32_e32 v16, 1.0, v17
	v_rcp_f32_e32 v16, v16
	v_lshlrev_b32_e32 v17, 16, v19
	v_mul_f32_e32 v15, v15, v17
	v_and_b32_e32 v17, 0xffff0000, v19
	v_mul_f32_e32 v16, v16, v17
	v_cvt_pk_bf16_f32 v15, v15, v16
	v_lshlrev_b32_e32 v16, 16, v20
	v_mul_f32_e32 v10, v10, v16
	v_and_b32_e32 v16, 0xffff0000, v20
	v_mul_f32_e32 v11, v11, v16
	v_cvt_pk_bf16_f32 v16, v10, v11
	v_add_f32_e32 v10, 1.0, v12
	v_rcp_f32_e32 v10, v10
	v_add_f32_e32 v11, 1.0, v13
	v_rcp_f32_e32 v11, v11
	v_lshlrev_b32_e32 v12, 16, v21
	v_mul_f32_e32 v10, v10, v12
	v_and_b32_e32 v12, 0xffff0000, v21
	v_mul_f32_e32 v11, v11, v12
	s_waitcnt vmcnt(0)
	v_lshlrev_b32_e32 v12, 16, v22
	v_mul_f32_e32 v6, v6, v12
	v_and_b32_e32 v12, 0xffff0000, v22
	v_mul_f32_e32 v7, v7, v12
	v_cvt_pk_bf16_f32 v6, v6, v7
	v_add_f32_e32 v7, 1.0, v8
	v_rcp_f32_e32 v7, v7
	v_add_f32_e32 v8, 1.0, v9
	v_rcp_f32_e32 v8, v8
	v_lshlrev_b32_e32 v9, 16, v23
	v_mul_f32_e32 v7, v7, v9
	v_and_b32_e32 v9, 0xffff0000, v23
	v_mul_f32_e32 v8, v8, v9
	v_cvt_pk_bf16_f32 v7, v7, v8
	v_lshlrev_b32_e32 v8, 16, v24
	v_mul_f32_e32 v2, v2, v8
	v_and_b32_e32 v8, 0xffff0000, v24
	v_mul_f32_e32 v3, v3, v8
	v_cvt_pk_bf16_f32 v8, v2, v3
	v_add_f32_e32 v2, 1.0, v4
	v_rcp_f32_e32 v2, v2
	v_add_f32_e32 v3, 1.0, v5
	v_rcp_f32_e32 v3, v3
	v_lshlrev_b32_e32 v4, 16, v25
	v_cvt_pk_bf16_f32 v17, v10, v11
	v_lshl_add_u64 v[10:11], s[6:7], 0, v[26:27]
	v_mul_f32_e32 v2, v2, v4
	v_and_b32_e32 v4, 0xffff0000, v25
	global_store_dwordx4 v[10:11], v[14:17], off
	v_mul_f32_e32 v3, v3, v4
	v_cvt_pk_bf16_f32 v9, v2, v3
	global_store_dwordx4 v[10:11], v[6:9], off offset:256
	s_cbranch_vccnz .LBB0_1504
	s_andn2_b64 vcc, exec, s[0:1]
	s_cbranch_vccnz .LBB0_1503
	s_barrier
	s_branch .LBB0_1503
